# v53 + redundant lgkmcnt waits removed from the MoE MFMA bursts as well
# baseline (speedup 1.0000x reference)
.LBB0_1175:
	s_waitcnt lgkmcnt(14)
	ds_read_b64_tr_b16 v[150:151], v214 offset:49152
	ds_read_b64_tr_b16 v[152:153], v214 offset:51200
	ds_read_b64_tr_b16 v[154:155], v217 offset:49152
	ds_read_b64_tr_b16 v[156:157], v217 offset:51200
	s_waitcnt lgkmcnt(14)
	ds_read_b64_tr_b16 v[158:159], v216 offset:49152
	ds_read_b64_tr_b16 v[160:161], v216 offset:51200
	ds_read_b64_tr_b16 v[162:163], v215 offset:49152
	ds_read_b64_tr_b16 v[164:165], v215 offset:51200
	v_add_u32_e32 v1, s98, v213
	s_waitcnt lgkmcnt(14)
	ds_read_b128 v[194:197], v1
	ds_read_b128 v[190:193], v1 offset:1024
	ds_read_b128 v[186:189], v1 offset:2048
	ds_read_b128 v[182:185], v1 offset:3072
	s_waitcnt lgkmcnt(14)
	ds_read_b128 v[178:181], v1 offset:4096
	ds_read_b128 v[174:177], v1 offset:5120
	ds_read_b128 v[170:173], v1 offset:6144
	ds_read_b128 v[166:169], v1 offset:7168
	s_mov_b32 m0, s99
	s_add_i32 s8, s99, 0x2000
	global_load_lds_dwordx4 v[206:207], off
	s_mov_b32 m0, s8
	s_add_i32 s8, s100, 0x2000
	global_load_lds_dwordx4 v[204:205], off
	s_mov_b32 m0, s100
	s_nop 0
	global_load_lds_dwordx4 v[206:207], off offset:64
	s_mov_b32 m0, s8
	s_nop 0
	global_load_lds_dwordx4 v[204:205], off offset:64
	v_add_u32_e32 v1, 0x10000, v218
	s_waitcnt vmcnt(8)
	v_cvt_pk_bf16_f32 v224, v224, v225
	v_cvt_pk_bf16_f32 v225, v226, v227
	v_cvt_pk_bf16_f32 v226, v228, v229
	v_cvt_pk_bf16_f32 v227, v230, v231
	ds_write_b128 v1, v[224:227]
	v_cvt_pk_bf16_f32 v232, v232, v233
	v_cvt_pk_bf16_f32 v233, v234, v235
	v_cvt_pk_bf16_f32 v234, v236, v237
	v_cvt_pk_bf16_f32 v235, v238, v239
	ds_write_b128 v1, v[232:235] offset:8192
	global_load_dwordx4 v[224:227], v[208:209], off
	global_load_dwordx4 v[228:231], v[208:209], off offset:16
	v_lshl_add_u64 v[4:5], v[208:209], 0, s[62:63]
	global_load_dwordx4 v[232:235], v[4:5], off
	global_load_dwordx4 v[236:239], v[4:5], off offset:16
	s_waitcnt lgkmcnt(0)
	s_barrier
	s_setprio 1
	v_cndmask_b32_e64 v1, 0, 1, s[76:77]
	v_cmp_ne_u32_e64 s[8:9], 1, v1
	s_andn2_b64 vcc, exec, s[76:77]
	s_cbranch_vccnz .Lmoe_end_even
	v_mfma_f32_16x16x32_bf16 v[146:149], v[150:153], v[194:197], v[146:149]
	v_mfma_f32_16x16x32_bf16 v[142:145], v[154:157], v[194:197], v[142:145]
	v_mfma_f32_16x16x32_bf16 v[138:141], v[158:161], v[194:197], v[138:141]
	v_mfma_f32_16x16x32_bf16 v[134:137], v[162:165], v[194:197], v[134:137]
	v_mfma_f32_16x16x32_bf16 v[130:133], v[150:153], v[190:193], v[130:133]
	v_mfma_f32_16x16x32_bf16 v[122:125], v[154:157], v[190:193], v[122:125]
	v_mfma_f32_16x16x32_bf16 v[126:129], v[158:161], v[190:193], v[126:129]
	v_mfma_f32_16x16x32_bf16 v[118:121], v[162:165], v[190:193], v[118:121]
	v_mfma_f32_16x16x32_bf16 v[114:117], v[150:153], v[186:189], v[114:117]
	v_mfma_f32_16x16x32_bf16 v[106:109], v[154:157], v[186:189], v[106:109]
	v_mfma_f32_16x16x32_bf16 v[110:113], v[158:161], v[186:189], v[110:113]
	v_mfma_f32_16x16x32_bf16 v[102:105], v[162:165], v[186:189], v[102:105]
	v_mfma_f32_16x16x32_bf16 v[98:101], v[150:153], v[182:185], v[98:101]
	v_mfma_f32_16x16x32_bf16 v[90:93], v[154:157], v[182:185], v[90:93]
	v_mfma_f32_16x16x32_bf16 v[94:97], v[158:161], v[182:185], v[94:97]
	v_mfma_f32_16x16x32_bf16 v[86:89], v[162:165], v[182:185], v[86:89]
	v_mfma_f32_16x16x32_bf16 v[82:85], v[150:153], v[178:181], v[82:85]
	v_mfma_f32_16x16x32_bf16 v[74:77], v[154:157], v[178:181], v[74:77]
	v_mfma_f32_16x16x32_bf16 v[78:81], v[158:161], v[178:181], v[78:81]
	v_mfma_f32_16x16x32_bf16 v[70:73], v[162:165], v[178:181], v[70:73]
	v_mfma_f32_16x16x32_bf16 v[66:69], v[150:153], v[174:177], v[66:69]
	v_mfma_f32_16x16x32_bf16 v[58:61], v[154:157], v[174:177], v[58:61]
	v_mfma_f32_16x16x32_bf16 v[62:65], v[158:161], v[174:177], v[62:65]
	v_mfma_f32_16x16x32_bf16 v[54:57], v[162:165], v[174:177], v[54:57]
	v_mfma_f32_16x16x32_bf16 v[50:53], v[150:153], v[170:173], v[50:53]
	v_mfma_f32_16x16x32_bf16 v[42:45], v[154:157], v[170:173], v[42:45]
	v_mfma_f32_16x16x32_bf16 v[46:49], v[158:161], v[170:173], v[46:49]
	v_mfma_f32_16x16x32_bf16 v[38:41], v[162:165], v[170:173], v[38:41]
	v_mfma_f32_16x16x32_bf16 v[34:37], v[150:153], v[166:169], v[34:37]
	v_mfma_f32_16x16x32_bf16 v[26:29], v[154:157], v[166:169], v[26:29]
	v_mfma_f32_16x16x32_bf16 v[30:33], v[158:161], v[166:169], v[30:33]
	v_mfma_f32_16x16x32_bf16 v[22:25], v[162:165], v[166:169], v[22:25]
.Lmoe_end_even:
	s_setprio 0
	s_add_i32 s34, s34, 1
	s_add_i32 s5, s5, 1
	s_and_b32 s5, s5, 3
	s_lshl_b32 s98, s5, 14
	s_cmp_eq_u32 s5, 3
	s_cselect_b32 s98, 0x18000, s98
	v_lshl_add_u64 v[204:205], v[204:205], 0, 64
	v_lshl_add_u64 v[206:207], v[206:207], 0, 64
	v_lshl_add_u64 v[208:209], v[208:209], 0, s[66:67]
	s_cmp_eq_u32 s34, 61
	s_waitcnt lgkmcnt(0)
	s_barrier
	s_cbranch_scc1 .Lmoe_t61
	s_waitcnt lgkmcnt(14)
	ds_read_b64_tr_b16 v[150:151], v240
	ds_read_b64_tr_b16 v[152:153], v240 offset:2048
	ds_read_b64_tr_b16 v[154:155], v241
	ds_read_b64_tr_b16 v[156:157], v241 offset:2048
	s_waitcnt lgkmcnt(14)
	ds_read_b64_tr_b16 v[158:159], v242
	ds_read_b64_tr_b16 v[160:161], v242 offset:2048
	ds_read_b64_tr_b16 v[162:163], v243
	ds_read_b64_tr_b16 v[164:165], v243 offset:2048
	v_add_u32_e32 v1, s98, v213
	s_waitcnt lgkmcnt(14)
	ds_read_b128 v[194:197], v1
	ds_read_b128 v[190:193], v1 offset:1024
	ds_read_b128 v[186:189], v1 offset:2048
	ds_read_b128 v[182:185], v1 offset:3072
	s_waitcnt lgkmcnt(14)
	ds_read_b128 v[178:181], v1 offset:4096
	ds_read_b128 v[174:177], v1 offset:5120
	ds_read_b128 v[170:173], v1 offset:6144
	ds_read_b128 v[166:169], v1 offset:7168
	v_add_u32_e32 v1, 0xc000, v218
	s_waitcnt vmcnt(6)
	v_cvt_pk_bf16_f32 v18, v18, v19
	v_cvt_pk_bf16_f32 v19, v20, v21
	v_cvt_pk_bf16_f32 v20, v14, v15
	v_cvt_pk_bf16_f32 v21, v16, v17
	ds_write_b128 v1, v[18:21]
	v_cvt_pk_bf16_f32 v4, v10, v11
	v_cvt_pk_bf16_f32 v5, v12, v13
	v_cvt_pk_bf16_f32 v6, v6, v7
	v_cvt_pk_bf16_f32 v7, v8, v9
	ds_write_b128 v1, v[4:7] offset:8192
	global_load_dwordx4 v[18:21], v[208:209], off
	global_load_dwordx4 v[14:17], v[208:209], off offset:16
	v_lshl_add_u64 v[4:5], v[208:209], 0, s[62:63]
	global_load_dwordx4 v[10:13], v[4:5], off
	global_load_dwordx4 v[6:9], v[4:5], off offset:16
	s_waitcnt lgkmcnt(0)
	s_barrier
	s_setprio 1
	v_cndmask_b32_e64 v1, 0, 1, s[76:77]
	v_cmp_ne_u32_e64 s[8:9], 1, v1
	s_andn2_b64 vcc, exec, s[76:77]
	s_cbranch_vccnz .LBB0_1174
	v_mfma_f32_16x16x32_bf16 v[146:149], v[150:153], v[194:197], v[146:149]
	v_mfma_f32_16x16x32_bf16 v[142:145], v[154:157], v[194:197], v[142:145]
	v_mfma_f32_16x16x32_bf16 v[138:141], v[158:161], v[194:197], v[138:141]
	v_mfma_f32_16x16x32_bf16 v[134:137], v[162:165], v[194:197], v[134:137]
	v_mfma_f32_16x16x32_bf16 v[130:133], v[150:153], v[190:193], v[130:133]
	v_mfma_f32_16x16x32_bf16 v[122:125], v[154:157], v[190:193], v[122:125]
	v_mfma_f32_16x16x32_bf16 v[126:129], v[158:161], v[190:193], v[126:129]
	v_mfma_f32_16x16x32_bf16 v[118:121], v[162:165], v[190:193], v[118:121]
	v_mfma_f32_16x16x32_bf16 v[114:117], v[150:153], v[186:189], v[114:117]
	v_mfma_f32_16x16x32_bf16 v[106:109], v[154:157], v[186:189], v[106:109]
	v_mfma_f32_16x16x32_bf16 v[110:113], v[158:161], v[186:189], v[110:113]
	v_mfma_f32_16x16x32_bf16 v[102:105], v[162:165], v[186:189], v[102:105]
	v_mfma_f32_16x16x32_bf16 v[98:101], v[150:153], v[182:185], v[98:101]
	v_mfma_f32_16x16x32_bf16 v[90:93], v[154:157], v[182:185], v[90:93]
	v_mfma_f32_16x16x32_bf16 v[94:97], v[158:161], v[182:185], v[94:97]
	v_mfma_f32_16x16x32_bf16 v[86:89], v[162:165], v[182:185], v[86:89]
	v_mfma_f32_16x16x32_bf16 v[82:85], v[150:153], v[178:181], v[82:85]
	v_mfma_f32_16x16x32_bf16 v[74:77], v[154:157], v[178:181], v[74:77]
	v_mfma_f32_16x16x32_bf16 v[78:81], v[158:161], v[178:181], v[78:81]
	v_mfma_f32_16x16x32_bf16 v[70:73], v[162:165], v[178:181], v[70:73]
	v_mfma_f32_16x16x32_bf16 v[66:69], v[150:153], v[174:177], v[66:69]
	v_mfma_f32_16x16x32_bf16 v[58:61], v[154:157], v[174:177], v[58:61]
	v_mfma_f32_16x16x32_bf16 v[62:65], v[158:161], v[174:177], v[62:65]
	v_mfma_f32_16x16x32_bf16 v[54:57], v[162:165], v[174:177], v[54:57]
	v_mfma_f32_16x16x32_bf16 v[50:53], v[150:153], v[170:173], v[50:53]
	v_mfma_f32_16x16x32_bf16 v[42:45], v[154:157], v[170:173], v[42:45]
	v_mfma_f32_16x16x32_bf16 v[46:49], v[158:161], v[170:173], v[46:49]
	v_mfma_f32_16x16x32_bf16 v[38:41], v[162:165], v[170:173], v[38:41]
	v_mfma_f32_16x16x32_bf16 v[34:37], v[150:153], v[166:169], v[34:37]
	v_mfma_f32_16x16x32_bf16 v[26:29], v[154:157], v[166:169], v[26:29]
	v_mfma_f32_16x16x32_bf16 v[30:33], v[158:161], v[166:169], v[30:33]
	v_mfma_f32_16x16x32_bf16 v[22:25], v[162:165], v[166:169], v[22:25]
	s_branch .LBB0_1174
.Lmoe_t61:
	s_waitcnt lgkmcnt(14)
	ds_read_b64_tr_b16 v[150:151], v240
	ds_read_b64_tr_b16 v[152:153], v240 offset:2048
	ds_read_b64_tr_b16 v[154:155], v241
	ds_read_b64_tr_b16 v[156:157], v241 offset:2048
	s_waitcnt lgkmcnt(14)
	ds_read_b64_tr_b16 v[158:159], v242
	ds_read_b64_tr_b16 v[160:161], v242 offset:2048
	ds_read_b64_tr_b16 v[162:163], v243
	ds_read_b64_tr_b16 v[164:165], v243 offset:2048
	v_add_u32_e32 v1, s98, v213
	s_waitcnt lgkmcnt(14)
	ds_read_b128 v[194:197], v1
	ds_read_b128 v[190:193], v1 offset:1024
	ds_read_b128 v[186:189], v1 offset:2048
	ds_read_b128 v[182:185], v1 offset:3072
	s_waitcnt lgkmcnt(14)
	ds_read_b128 v[178:181], v1 offset:4096
	ds_read_b128 v[174:177], v1 offset:5120
	ds_read_b128 v[170:173], v1 offset:6144
	ds_read_b128 v[166:169], v1 offset:7168
	v_add_u32_e32 v1, 0xc000, v218
	s_waitcnt vmcnt(6)
	v_cvt_pk_bf16_f32 v18, v18, v19
	v_cvt_pk_bf16_f32 v19, v20, v21
	v_cvt_pk_bf16_f32 v20, v14, v15
	v_cvt_pk_bf16_f32 v21, v16, v17
	ds_write_b128 v1, v[18:21]
	v_cvt_pk_bf16_f32 v4, v10, v11
	v_cvt_pk_bf16_f32 v5, v12, v13
	v_cvt_pk_bf16_f32 v6, v6, v7
	v_cvt_pk_bf16_f32 v7, v8, v9
	ds_write_b128 v1, v[4:7] offset:8192
	s_waitcnt lgkmcnt(0)
	s_barrier
	s_setprio 1
	v_cndmask_b32_e64 v1, 0, 1, s[76:77]
	v_cmp_ne_u32_e64 s[8:9], 1, v1
	s_andn2_b64 vcc, exec, s[76:77]
	s_cbranch_vccnz .Lmoe_end_t61
	v_mfma_f32_16x16x32_bf16 v[146:149], v[150:153], v[194:197], v[146:149]
	v_mfma_f32_16x16x32_bf16 v[142:145], v[154:157], v[194:197], v[142:145]
	v_mfma_f32_16x16x32_bf16 v[138:141], v[158:161], v[194:197], v[138:141]
	v_mfma_f32_16x16x32_bf16 v[134:137], v[162:165], v[194:197], v[134:137]
	v_mfma_f32_16x16x32_bf16 v[130:133], v[150:153], v[190:193], v[130:133]
	v_mfma_f32_16x16x32_bf16 v[122:125], v[154:157], v[190:193], v[122:125]
	v_mfma_f32_16x16x32_bf16 v[126:129], v[158:161], v[190:193], v[126:129]
	v_mfma_f32_16x16x32_bf16 v[118:121], v[162:165], v[190:193], v[118:121]
	v_mfma_f32_16x16x32_bf16 v[114:117], v[150:153], v[186:189], v[114:117]
	v_mfma_f32_16x16x32_bf16 v[106:109], v[154:157], v[186:189], v[106:109]
	v_mfma_f32_16x16x32_bf16 v[110:113], v[158:161], v[186:189], v[110:113]
	v_mfma_f32_16x16x32_bf16 v[102:105], v[162:165], v[186:189], v[102:105]
	v_mfma_f32_16x16x32_bf16 v[98:101], v[150:153], v[182:185], v[98:101]
	v_mfma_f32_16x16x32_bf16 v[90:93], v[154:157], v[182:185], v[90:93]
	v_mfma_f32_16x16x32_bf16 v[94:97], v[158:161], v[182:185], v[94:97]
	v_mfma_f32_16x16x32_bf16 v[86:89], v[162:165], v[182:185], v[86:89]
	v_mfma_f32_16x16x32_bf16 v[82:85], v[150:153], v[178:181], v[82:85]
	v_mfma_f32_16x16x32_bf16 v[74:77], v[154:157], v[178:181], v[74:77]
	v_mfma_f32_16x16x32_bf16 v[78:81], v[158:161], v[178:181], v[78:81]
	v_mfma_f32_16x16x32_bf16 v[70:73], v[162:165], v[178:181], v[70:73]
	v_mfma_f32_16x16x32_bf16 v[66:69], v[150:153], v[174:177], v[66:69]
	v_mfma_f32_16x16x32_bf16 v[58:61], v[154:157], v[174:177], v[58:61]
	v_mfma_f32_16x16x32_bf16 v[62:65], v[158:161], v[174:177], v[62:65]
	v_mfma_f32_16x16x32_bf16 v[54:57], v[162:165], v[174:177], v[54:57]
	v_mfma_f32_16x16x32_bf16 v[50:53], v[150:153], v[170:173], v[50:53]
	v_mfma_f32_16x16x32_bf16 v[42:45], v[154:157], v[170:173], v[42:45]
	v_mfma_f32_16x16x32_bf16 v[46:49], v[158:161], v[170:173], v[46:49]
	v_mfma_f32_16x16x32_bf16 v[38:41], v[162:165], v[170:173], v[38:41]
	v_mfma_f32_16x16x32_bf16 v[34:37], v[150:153], v[166:169], v[34:37]
	v_mfma_f32_16x16x32_bf16 v[26:29], v[154:157], v[166:169], v[26:29]
	v_mfma_f32_16x16x32_bf16 v[30:33], v[158:161], v[166:169], v[30:33]
	v_mfma_f32_16x16x32_bf16 v[22:25], v[162:165], v[166:169], v[22:25]
